# GEMM load phases: LDS-DMA loads issued before the ds_read burst of the same phase (on v40)
# baseline (speedup 1.0000x reference)
.LBB3_34:
	s_mov_b32 m0, s66
	s_nop 0
	global_load_lds_dwordx4 v60, s[68:69]
	s_add_i32 m0, s66, 0x2000
	s_nop 0
	global_load_lds_dwordx4 v62, s[68:69]
	ds_read_b128 v[98:101], v94 offset:16384
	ds_read_b128 v[102:105], v94 offset:17408
	ds_read_b128 v[106:109], v94 offset:18432
	ds_read_b128 v[110:113], v94 offset:19456
	ds_read_b128 v[114:117], v95
	ds_read_b128 v[118:121], v95 offset:1024
	ds_read_b128 v[122:125], v95 offset:2048
	ds_read_b128 v[126:129], v95 offset:3072
	ds_read_b128 v[130:133], v95 offset:4096
	ds_read_b128 v[134:137], v95 offset:5120
	ds_read_b128 v[138:141], v95 offset:6144
	ds_read_b128 v[142:145], v95 offset:7168
	s_barrier
	s_setprio 1
	s_waitcnt lgkmcnt(7)
	v_mfma_f32_16x16x32_f16 v[44:47], v[98:101], v[114:117], v[44:47]
	v_mfma_f32_16x16x32_f16 v[40:43], v[106:109], v[114:117], v[40:43]
	s_waitcnt lgkmcnt(5)
	v_mfma_f32_16x16x32_f16 v[32:35], v[98:101], v[122:125], v[32:35]
	v_mfma_f32_16x16x32_f16 v[28:31], v[106:109], v[122:125], v[28:31]
	s_waitcnt lgkmcnt(3)
	v_mfma_f32_16x16x32_f16 v[20:23], v[98:101], v[130:133], v[20:23]
	v_mfma_f32_16x16x32_f16 v[16:19], v[106:109], v[130:133], v[16:19]
	s_waitcnt lgkmcnt(1)
	v_mfma_f32_16x16x32_f16 v[8:11], v[98:101], v[138:141], v[8:11]
	v_mfma_f32_16x16x32_f16 v[4:7], v[106:109], v[138:141], v[4:7]
	v_mfma_f32_16x16x32_f16 v[44:47], v[102:105], v[118:121], v[44:47]
	v_mfma_f32_16x16x32_f16 v[40:43], v[110:113], v[118:121], v[40:43]
	v_mfma_f32_16x16x32_f16 v[32:35], v[102:105], v[126:129], v[32:35]
	v_mfma_f32_16x16x32_f16 v[28:31], v[110:113], v[126:129], v[28:31]
	v_mfma_f32_16x16x32_f16 v[20:23], v[102:105], v[134:137], v[20:23]
	v_mfma_f32_16x16x32_f16 v[16:19], v[110:113], v[134:137], v[16:19]
	s_waitcnt lgkmcnt(0)
	v_mfma_f32_16x16x32_f16 v[8:11], v[102:105], v[142:145], v[8:11]
	v_mfma_f32_16x16x32_f16 v[4:7], v[110:113], v[142:145], v[4:7]
	s_setprio 0
	s_barrier
	s_add_i32 m0, s43, 0x18000
	s_nop 0
	global_load_lds_dwordx4 v64, s[70:71]
	s_add_i32 m0, s43, 0x1a000
	s_nop 0
	global_load_lds_dwordx4 v66, s[70:71]
	s_add_i32 m0, s43, 0x1c000
	s_nop 0
	global_load_lds_dwordx4 v68, s[70:71]
	ds_read_b128 v[98:101], v94 offset:20480
	ds_read_b128 v[102:105], v94 offset:21504
	s_waitcnt vmcnt(5)
	s_barrier
	s_setprio 1
	s_waitcnt lgkmcnt(1)
	v_mfma_f32_16x16x32_f16 v[36:39], v[98:101], v[114:117], v[36:39]
	v_mfma_f32_16x16x32_f16 v[24:27], v[98:101], v[122:125], v[24:27]
	v_mfma_f32_16x16x32_f16 v[12:15], v[98:101], v[130:133], v[12:15]
	v_mfma_f32_16x16x32_f16 v[0:3], v[98:101], v[138:141], v[0:3]
	s_waitcnt lgkmcnt(0)
	v_mfma_f32_16x16x32_f16 v[36:39], v[102:105], v[118:121], v[36:39]
	v_mfma_f32_16x16x32_f16 v[24:27], v[102:105], v[126:129], v[24:27]
	v_mfma_f32_16x16x32_f16 v[12:15], v[102:105], v[134:137], v[12:15]
	v_mfma_f32_16x16x32_f16 v[0:3], v[102:105], v[142:145], v[0:3]
	s_setprio 0
	s_barrier
	s_mov_b32 m0, s43
	s_nop 0
	global_load_lds_dwordx4 v48, s[64:65]
	s_mov_b32 m0, s44
	s_nop 0
	global_load_lds_dwordx4 v52, s[64:65]
	ds_read_b128 v[98:101], v94 offset:57344
	ds_read_b128 v[102:105], v94 offset:58368
	ds_read_b128 v[106:109], v94 offset:59392
	ds_read_b128 v[110:113], v94 offset:60416
	ds_read_b128 v[114:117], v95 offset:40960
	ds_read_b128 v[118:121], v95 offset:41984
	ds_read_b128 v[122:125], v95 offset:43008
	ds_read_b128 v[126:129], v95 offset:44032
	ds_read_b128 v[130:133], v95 offset:45056
	ds_read_b128 v[134:137], v95 offset:46080
	ds_read_b128 v[138:141], v95 offset:47104
	ds_read_b128 v[142:145], v95 offset:48128
	s_barrier
	s_setprio 1
	s_waitcnt lgkmcnt(7)
	v_mfma_f32_16x16x32_f16 v[44:47], v[98:101], v[114:117], v[44:47]
	v_mfma_f32_16x16x32_f16 v[40:43], v[106:109], v[114:117], v[40:43]
	s_waitcnt lgkmcnt(5)
	v_mfma_f32_16x16x32_f16 v[32:35], v[98:101], v[122:125], v[32:35]
	v_mfma_f32_16x16x32_f16 v[28:31], v[106:109], v[122:125], v[28:31]
	s_waitcnt lgkmcnt(3)
	v_mfma_f32_16x16x32_f16 v[20:23], v[98:101], v[130:133], v[20:23]
	v_mfma_f32_16x16x32_f16 v[16:19], v[106:109], v[130:133], v[16:19]
	s_waitcnt lgkmcnt(1)
	v_mfma_f32_16x16x32_f16 v[8:11], v[98:101], v[138:141], v[8:11]
	v_mfma_f32_16x16x32_f16 v[4:7], v[106:109], v[138:141], v[4:7]
	v_mfma_f32_16x16x32_f16 v[44:47], v[102:105], v[118:121], v[44:47]
	v_mfma_f32_16x16x32_f16 v[40:43], v[110:113], v[118:121], v[40:43]
	v_mfma_f32_16x16x32_f16 v[32:35], v[102:105], v[126:129], v[32:35]
	v_mfma_f32_16x16x32_f16 v[28:31], v[110:113], v[126:129], v[28:31]
	v_mfma_f32_16x16x32_f16 v[20:23], v[102:105], v[134:137], v[20:23]
	v_mfma_f32_16x16x32_f16 v[16:19], v[110:113], v[134:137], v[16:19]
	s_waitcnt lgkmcnt(0)
	v_mfma_f32_16x16x32_f16 v[8:11], v[102:105], v[142:145], v[8:11]
	v_mfma_f32_16x16x32_f16 v[4:7], v[110:113], v[142:145], v[4:7]
	s_setprio 0
	s_barrier
	s_mov_b32 m0, s45
	s_nop 0
	global_load_lds_dwordx4 v50, s[26:27]
	s_mov_b32 m0, s46
	s_nop 0
	global_load_lds_dwordx4 v54, s[26:27]
	s_mov_b32 m0, s47
	s_nop 0
	global_load_lds_dwordx4 v56, s[26:27]
	ds_read_b128 v[98:101], v94 offset:61440
	ds_read_b128 v[102:105], v94 offset:62464
	s_waitcnt vmcnt(5)
	s_barrier
	s_setprio 1
	s_waitcnt lgkmcnt(1)
	v_mfma_f32_16x16x32_f16 v[36:39], v[98:101], v[114:117], v[36:39]
	v_mfma_f32_16x16x32_f16 v[24:27], v[98:101], v[122:125], v[24:27]
	v_mfma_f32_16x16x32_f16 v[12:15], v[98:101], v[130:133], v[12:15]
	v_mfma_f32_16x16x32_f16 v[0:3], v[98:101], v[138:141], v[0:3]
	s_waitcnt lgkmcnt(0)
	v_mfma_f32_16x16x32_f16 v[36:39], v[102:105], v[118:121], v[36:39]
	v_mfma_f32_16x16x32_f16 v[24:27], v[102:105], v[126:129], v[24:27]
	v_mfma_f32_16x16x32_f16 v[12:15], v[102:105], v[134:137], v[12:15]
	v_mfma_f32_16x16x32_f16 v[0:3], v[102:105], v[142:145], v[0:3]
	s_setprio 0
	s_barrier
	s_mov_b32 m0, s52
	s_nop 0
	global_load_lds_dwordx4 v48, s[72:73]
	s_mov_b32 m0, s53
	s_nop 0
	global_load_lds_dwordx4 v52, s[72:73]
	ds_read_b128 v[98:101], v96
	ds_read_b128 v[102:105], v96 offset:1024
	ds_read_b128 v[106:109], v96 offset:2048
	ds_read_b128 v[110:113], v96 offset:3072
	ds_read_b128 v[114:117], v97
	ds_read_b128 v[118:121], v97 offset:1024
	ds_read_b128 v[122:125], v97 offset:2048
	ds_read_b128 v[126:129], v97 offset:3072
	ds_read_b128 v[130:133], v97 offset:4096
	ds_read_b128 v[134:137], v97 offset:5120
	ds_read_b128 v[138:141], v97 offset:6144
	ds_read_b128 v[142:145], v97 offset:7168
	s_barrier
	s_setprio 1
	s_waitcnt lgkmcnt(7)
	v_mfma_f32_16x16x32_f16 v[44:47], v[98:101], v[114:117], v[44:47]
	v_mfma_f32_16x16x32_f16 v[40:43], v[106:109], v[114:117], v[40:43]
	s_waitcnt lgkmcnt(5)
	v_mfma_f32_16x16x32_f16 v[32:35], v[98:101], v[122:125], v[32:35]
	v_mfma_f32_16x16x32_f16 v[28:31], v[106:109], v[122:125], v[28:31]
	s_waitcnt lgkmcnt(3)
	v_mfma_f32_16x16x32_f16 v[20:23], v[98:101], v[130:133], v[20:23]
	v_mfma_f32_16x16x32_f16 v[16:19], v[106:109], v[130:133], v[16:19]
	s_waitcnt lgkmcnt(1)
	v_mfma_f32_16x16x32_f16 v[8:11], v[98:101], v[138:141], v[8:11]
	v_mfma_f32_16x16x32_f16 v[4:7], v[106:109], v[138:141], v[4:7]
	v_mfma_f32_16x16x32_f16 v[44:47], v[102:105], v[118:121], v[44:47]
	v_mfma_f32_16x16x32_f16 v[40:43], v[110:113], v[118:121], v[40:43]
	v_mfma_f32_16x16x32_f16 v[32:35], v[102:105], v[126:129], v[32:35]
	v_mfma_f32_16x16x32_f16 v[28:31], v[110:113], v[126:129], v[28:31]
	v_mfma_f32_16x16x32_f16 v[20:23], v[102:105], v[134:137], v[20:23]
	v_mfma_f32_16x16x32_f16 v[16:19], v[110:113], v[134:137], v[16:19]
	s_waitcnt lgkmcnt(0)
	v_mfma_f32_16x16x32_f16 v[8:11], v[102:105], v[142:145], v[8:11]
	v_mfma_f32_16x16x32_f16 v[4:7], v[110:113], v[142:145], v[4:7]
	s_setprio 0
	s_barrier
	s_mov_b32 m0, s54
	s_nop 0
	global_load_lds_dwordx4 v50, s[74:75]
	s_add_i32 m0, s54, 0x2000
	s_nop 0
	global_load_lds_dwordx4 v54, s[74:75]
	s_add_i32 m0, s54, 0x4000
	s_nop 0
	global_load_lds_dwordx4 v56, s[74:75]
	ds_read_b128 v[98:101], v96 offset:4096
	ds_read_b128 v[102:105], v96 offset:5120
	s_waitcnt vmcnt(5)
	s_barrier
	s_setprio 1
	s_waitcnt lgkmcnt(1)
	v_mfma_f32_16x16x32_f16 v[36:39], v[98:101], v[114:117], v[36:39]
	v_mfma_f32_16x16x32_f16 v[24:27], v[98:101], v[122:125], v[24:27]
	v_mfma_f32_16x16x32_f16 v[12:15], v[98:101], v[130:133], v[12:15]
	v_mfma_f32_16x16x32_f16 v[0:3], v[98:101], v[138:141], v[0:3]
	s_waitcnt lgkmcnt(0)
	v_mfma_f32_16x16x32_f16 v[36:39], v[102:105], v[118:121], v[36:39]
	v_mfma_f32_16x16x32_f16 v[24:27], v[102:105], v[126:129], v[24:27]
	v_mfma_f32_16x16x32_f16 v[12:15], v[102:105], v[134:137], v[12:15]
	v_mfma_f32_16x16x32_f16 v[0:3], v[102:105], v[142:145], v[0:3]
	s_setprio 0
	s_add_i32 s63, s63, 3
	s_add_u32 s24, s24, 0x180
	s_addc_u32 s25, s25, 0
	s_cmp_ge_i32 s63, s49
	s_cbranch_scc1 .Lrot_exit_qkv
	s_add_u32 s68, s20, s24
	s_addc_u32 s69, s21, s25
	s_add_u32 s70, s22, s24
	s_addc_u32 s71, s23, s25
	s_add_u32 s26, s20, s24
	s_addc_u32 s27, s21, s25
	s_add_u32 s26, s26, 0x180
	s_addc_u32 s27, s27, 0
	s_add_u32 s64, s22, s24
	s_addc_u32 s65, s23, s25
	s_add_u32 s66, s64, 0x180
	s_addc_u32 s67, s65, 0
	s_cmp_eq_u32 s56, s63
	s_cselect_b32 s65, s5, s27
	s_cselect_b32 s64, s4, s26
	s_cselect_b32 s27, s7, s67
	s_cselect_b32 s26, s6, s66
	s_add_u32 s72, s64, 0x80
	s_addc_u32 s73, s65, 0
	s_add_u32 s74, s26, 0x80
	s_addc_u32 s75, s27, 0
	s_add_i32 s66, s58, s38
	s_barrier
	s_branch .LBB3_34

.LBB4_22:
	s_mov_b32 m0, s70
	s_nop 0
	global_load_lds_dwordx4 v0, s[74:75]
	s_add_i32 m0, s70, 0x2000
	s_nop 0
	global_load_lds_dwordx4 v120, s[74:75]
	ds_read_b128 v[130:133], v136 offset:16384
	ds_read_b128 v[142:145], v136 offset:17408
	ds_read_b128 v[146:149], v136 offset:18432
	ds_read_b128 v[150:153], v136 offset:19456
	ds_read_b128 v[154:157], v137
	ds_read_b128 v[158:161], v137 offset:1024
	ds_read_b128 v[162:165], v137 offset:2048
	ds_read_b128 v[166:169], v137 offset:3072
	ds_read_b128 v[170:173], v137 offset:4096
	ds_read_b128 v[174:177], v137 offset:5120
	ds_read_b128 v[178:181], v137 offset:6144
	ds_read_b128 v[182:185], v137 offset:7168
	s_barrier
	s_setprio 1
	s_waitcnt lgkmcnt(7)
	v_mfma_f32_16x16x32_f16 v[94:97], v[130:133], v[154:157], v[94:97]
	v_mfma_f32_16x16x32_f16 v[90:93], v[146:149], v[154:157], v[90:93]
	s_waitcnt lgkmcnt(5)
	v_mfma_f32_16x16x32_f16 v[82:85], v[130:133], v[162:165], v[82:85]
	v_mfma_f32_16x16x32_f16 v[78:81], v[146:149], v[162:165], v[78:81]
	s_waitcnt lgkmcnt(3)
	v_mfma_f32_16x16x32_f16 v[70:73], v[130:133], v[170:173], v[70:73]
	v_mfma_f32_16x16x32_f16 v[66:69], v[146:149], v[170:173], v[66:69]
	s_waitcnt lgkmcnt(1)
	v_mfma_f32_16x16x32_f16 v[58:61], v[130:133], v[178:181], v[58:61]
	v_mfma_f32_16x16x32_f16 v[54:57], v[146:149], v[178:181], v[54:57]
	v_mfma_f32_16x16x32_f16 v[94:97], v[142:145], v[158:161], v[94:97]
	v_mfma_f32_16x16x32_f16 v[90:93], v[150:153], v[158:161], v[90:93]
	v_mfma_f32_16x16x32_f16 v[82:85], v[142:145], v[166:169], v[82:85]
	v_mfma_f32_16x16x32_f16 v[78:81], v[150:153], v[166:169], v[78:81]
	v_mfma_f32_16x16x32_f16 v[70:73], v[142:145], v[174:177], v[70:73]
	v_mfma_f32_16x16x32_f16 v[66:69], v[150:153], v[174:177], v[66:69]
	s_waitcnt lgkmcnt(0)
	v_mfma_f32_16x16x32_f16 v[58:61], v[142:145], v[182:185], v[58:61]
	v_mfma_f32_16x16x32_f16 v[54:57], v[150:153], v[182:185], v[54:57]
	s_setprio 0
	s_barrier
	s_add_i32 m0, s49, 0x18000
	s_nop 0
	global_load_lds_dwordx4 v122, s[76:77]
	s_add_i32 m0, s49, 0x1a000
	s_nop 0
	global_load_lds_dwordx4 v124, s[76:77]
	s_add_i32 m0, s49, 0x1c000
	s_nop 0
	global_load_lds_dwordx4 v126, s[76:77]
	ds_read_b128 v[130:133], v136 offset:20480
	ds_read_b128 v[142:145], v136 offset:21504
	s_cmp_lg_u32 s67, 0
	s_cbranch_scc1 .Lpj_norm_0
	s_mul_i32 s72, s66, 0xc0
	v_add_u32_e32 v214, s72, v135
	v_ashrrev_i32_e32 v215, 31, v214
	v_lshl_add_u64 v[214:215], v[214:215], 2, s[10:11]
	global_load_dwordx4 v[202:205], v[214:215], off
	global_load_dwordx4 v[206:209], v[214:215], off offset:64
	global_load_dwordx4 v[210:213], v[214:215], off offset:128
	global_load_dwordx4 v[2:5], v[194:195], off
	global_load_dwordx4 v[6:9], v[194:195], off offset:64
	global_load_dwordx4 v[10:13], v[194:195], off offset:128
	global_load_dwordx4 v[14:17], v[196:197], off
	s_waitcnt vmcnt(12)
	s_branch .Lpj_join_0

.Lpj_join_0:
	s_barrier
	s_setprio 1
	s_waitcnt lgkmcnt(1)
	v_mfma_f32_16x16x32_f16 v[86:89], v[130:133], v[154:157], v[86:89]
	v_mfma_f32_16x16x32_f16 v[74:77], v[130:133], v[162:165], v[74:77]
	v_mfma_f32_16x16x32_f16 v[62:65], v[130:133], v[170:173], v[62:65]
	v_mfma_f32_16x16x32_f16 v[50:53], v[130:133], v[178:181], v[50:53]
	s_waitcnt lgkmcnt(0)
	v_mfma_f32_16x16x32_f16 v[86:89], v[142:145], v[158:161], v[86:89]
	v_mfma_f32_16x16x32_f16 v[74:77], v[142:145], v[166:169], v[74:77]
	v_mfma_f32_16x16x32_f16 v[62:65], v[142:145], v[174:177], v[62:65]
	v_mfma_f32_16x16x32_f16 v[50:53], v[142:145], v[182:185], v[50:53]
	s_setprio 0
	s_barrier
	s_mov_b32 m0, s49
	s_nop 0
	global_load_lds_dwordx4 v110, s[68:69]
	s_mov_b32 m0, s50
	s_nop 0
	global_load_lds_dwordx4 v114, s[68:69]
	ds_read_b128 v[130:133], v136 offset:57344
	ds_read_b128 v[142:145], v136 offset:58368
	ds_read_b128 v[146:149], v136 offset:59392
	ds_read_b128 v[150:153], v136 offset:60416
	ds_read_b128 v[154:157], v137 offset:40960
	ds_read_b128 v[158:161], v137 offset:41984
	ds_read_b128 v[162:165], v137 offset:43008
	ds_read_b128 v[166:169], v137 offset:44032
	ds_read_b128 v[170:173], v137 offset:45056
	ds_read_b128 v[174:177], v137 offset:46080
	ds_read_b128 v[178:181], v137 offset:47104
	ds_read_b128 v[182:185], v137 offset:48128
	s_barrier
	s_setprio 1
	s_waitcnt lgkmcnt(7)
	v_mfma_f32_16x16x32_f16 v[94:97], v[130:133], v[154:157], v[94:97]
	v_mfma_f32_16x16x32_f16 v[90:93], v[146:149], v[154:157], v[90:93]
	s_waitcnt lgkmcnt(5)
	v_mfma_f32_16x16x32_f16 v[82:85], v[130:133], v[162:165], v[82:85]
	v_mfma_f32_16x16x32_f16 v[78:81], v[146:149], v[162:165], v[78:81]
	s_waitcnt lgkmcnt(3)
	v_mfma_f32_16x16x32_f16 v[70:73], v[130:133], v[170:173], v[70:73]
	v_mfma_f32_16x16x32_f16 v[66:69], v[146:149], v[170:173], v[66:69]
	s_waitcnt lgkmcnt(1)
	v_mfma_f32_16x16x32_f16 v[58:61], v[130:133], v[178:181], v[58:61]
	v_mfma_f32_16x16x32_f16 v[54:57], v[146:149], v[178:181], v[54:57]
	v_mfma_f32_16x16x32_f16 v[94:97], v[142:145], v[158:161], v[94:97]
	v_mfma_f32_16x16x32_f16 v[90:93], v[150:153], v[158:161], v[90:93]
	v_mfma_f32_16x16x32_f16 v[82:85], v[142:145], v[166:169], v[82:85]
	v_mfma_f32_16x16x32_f16 v[78:81], v[150:153], v[166:169], v[78:81]
	v_mfma_f32_16x16x32_f16 v[70:73], v[142:145], v[174:177], v[70:73]
	v_mfma_f32_16x16x32_f16 v[66:69], v[150:153], v[174:177], v[66:69]
	s_waitcnt lgkmcnt(0)
	v_mfma_f32_16x16x32_f16 v[58:61], v[142:145], v[182:185], v[58:61]
	v_mfma_f32_16x16x32_f16 v[54:57], v[150:153], v[182:185], v[54:57]
	s_setprio 0
	s_barrier
	s_mov_b32 m0, s51
	s_nop 0
	global_load_lds_dwordx4 v112, s[34:35]
	s_mov_b32 m0, s52
	s_nop 0
	global_load_lds_dwordx4 v116, s[34:35]
	s_mov_b32 m0, s53
	s_nop 0
	global_load_lds_dwordx4 v118, s[34:35]
	ds_read_b128 v[130:133], v136 offset:61440
	ds_read_b128 v[142:145], v136 offset:62464
	s_cmp_lg_u32 s67, 0
	s_cbranch_scc1 .Lpj_norm_1
	global_load_dwordx4 v[18:21], v[196:197], off offset:64
	global_load_dwordx4 v[22:25], v[196:197], off offset:128
	global_load_dwordx4 v[26:29], v[198:199], off
	global_load_dwordx4 v[30:33], v[198:199], off offset:64
	s_waitcnt vmcnt(16)
	s_branch .Lpj_join_1

.Lpj_join_1:
	s_barrier
	s_setprio 1
	s_waitcnt lgkmcnt(1)
	v_mfma_f32_16x16x32_f16 v[86:89], v[130:133], v[154:157], v[86:89]
	v_mfma_f32_16x16x32_f16 v[74:77], v[130:133], v[162:165], v[74:77]
	v_mfma_f32_16x16x32_f16 v[62:65], v[130:133], v[170:173], v[62:65]
	v_mfma_f32_16x16x32_f16 v[50:53], v[130:133], v[178:181], v[50:53]
	s_waitcnt lgkmcnt(0)
	v_mfma_f32_16x16x32_f16 v[86:89], v[142:145], v[158:161], v[86:89]
	v_mfma_f32_16x16x32_f16 v[74:77], v[142:145], v[166:169], v[74:77]
	v_mfma_f32_16x16x32_f16 v[62:65], v[142:145], v[174:177], v[62:65]
	v_mfma_f32_16x16x32_f16 v[50:53], v[142:145], v[182:185], v[50:53]
	s_setprio 0
	s_barrier
	s_mov_b32 m0, s56
	s_nop 0
	global_load_lds_dwordx4 v110, s[78:79]
	s_mov_b32 m0, s57
	s_nop 0
	global_load_lds_dwordx4 v114, s[78:79]
	ds_read_b128 v[130:133], v138
	ds_read_b128 v[142:145], v138 offset:1024
	ds_read_b128 v[146:149], v138 offset:2048
	ds_read_b128 v[150:153], v138 offset:3072
	ds_read_b128 v[154:157], v139
	ds_read_b128 v[158:161], v139 offset:1024
	ds_read_b128 v[162:165], v139 offset:2048
	ds_read_b128 v[166:169], v139 offset:3072
	ds_read_b128 v[170:173], v139 offset:4096
	ds_read_b128 v[174:177], v139 offset:5120
	ds_read_b128 v[178:181], v139 offset:6144
	ds_read_b128 v[182:185], v139 offset:7168
	s_barrier
	s_setprio 1
	s_waitcnt lgkmcnt(7)
	v_mfma_f32_16x16x32_f16 v[94:97], v[130:133], v[154:157], v[94:97]
	v_mfma_f32_16x16x32_f16 v[90:93], v[146:149], v[154:157], v[90:93]
	s_waitcnt lgkmcnt(5)
	v_mfma_f32_16x16x32_f16 v[82:85], v[130:133], v[162:165], v[82:85]
	v_mfma_f32_16x16x32_f16 v[78:81], v[146:149], v[162:165], v[78:81]
	s_waitcnt lgkmcnt(3)
	v_mfma_f32_16x16x32_f16 v[70:73], v[130:133], v[170:173], v[70:73]
	v_mfma_f32_16x16x32_f16 v[66:69], v[146:149], v[170:173], v[66:69]
	s_waitcnt lgkmcnt(1)
	v_mfma_f32_16x16x32_f16 v[58:61], v[130:133], v[178:181], v[58:61]
	v_mfma_f32_16x16x32_f16 v[54:57], v[146:149], v[178:181], v[54:57]
	v_mfma_f32_16x16x32_f16 v[94:97], v[142:145], v[158:161], v[94:97]
	v_mfma_f32_16x16x32_f16 v[90:93], v[150:153], v[158:161], v[90:93]
	v_mfma_f32_16x16x32_f16 v[82:85], v[142:145], v[166:169], v[82:85]
	v_mfma_f32_16x16x32_f16 v[78:81], v[150:153], v[166:169], v[78:81]
	v_mfma_f32_16x16x32_f16 v[70:73], v[142:145], v[174:177], v[70:73]
	v_mfma_f32_16x16x32_f16 v[66:69], v[150:153], v[174:177], v[66:69]
	s_waitcnt lgkmcnt(0)
	v_mfma_f32_16x16x32_f16 v[58:61], v[142:145], v[182:185], v[58:61]
	v_mfma_f32_16x16x32_f16 v[54:57], v[150:153], v[182:185], v[54:57]
	s_setprio 0
	s_barrier
	s_mov_b32 m0, s58
	s_nop 0
	global_load_lds_dwordx4 v112, s[80:81]
	s_add_i32 m0, s58, 0x2000
	s_nop 0
	global_load_lds_dwordx4 v116, s[80:81]
	s_add_i32 m0, s58, 0x4000
	s_nop 0
	global_load_lds_dwordx4 v118, s[80:81]
	ds_read_b128 v[130:133], v138 offset:4096
	ds_read_b128 v[142:145], v138 offset:5120
	s_cmp_lg_u32 s67, 0
	s_cbranch_scc1 .Lpj_norm_2
	global_load_dwordx4 v[34:37], v[198:199], off offset:128
	global_load_dwordx4 v[38:41], v[200:201], off
	global_load_dwordx4 v[42:45], v[200:201], off offset:64
	global_load_dwordx4 v[46:49], v[200:201], off offset:128
	s_waitcnt vmcnt(13)
	s_branch .Lpj_join_2

.LBB5_55:
	s_mov_b32 m0, s76
	s_nop 0
	global_load_lds_dwordx4 v112, s[78:79]
	s_add_i32 m0, s76, 0x2000
	s_add_i32 s76, s27, s54
	global_load_lds_dwordx4 v114, s[78:79]
	s_mov_b32 m0, s76
	s_nop 0
	global_load_lds_dwordx4 v116, s[80:81]
	s_add_i32 m0, s76, 0x2000
	s_nop 0
	global_load_lds_dwordx4 v118, s[80:81]
	ds_read_b128 v[44:47], v130 offset:16384
	ds_read_b128 v[56:59], v130 offset:17408
	ds_read_b128 v[60:63], v130 offset:18432
	ds_read_b128 v[64:67], v130 offset:19456
	ds_read_b128 v[68:71], v131
	ds_read_b128 v[96:99], v131 offset:1024
	ds_read_b128 v[136:139], v131 offset:2048
	ds_read_b128 v[140:143], v131 offset:3072
	ds_read_b128 v[144:147], v131 offset:4096
	ds_read_b128 v[148:151], v131 offset:5120
	ds_read_b128 v[152:155], v131 offset:6144
	ds_read_b128 v[156:159], v131 offset:7168
	s_barrier
	s_setprio 1
	s_waitcnt lgkmcnt(7)
	v_mfma_f32_16x16x32_f16 v[92:95], v[44:47], v[68:71], v[92:95]
	v_mfma_f32_16x16x32_f16 v[88:91], v[60:63], v[68:71], v[88:91]
	s_waitcnt lgkmcnt(5)
	v_mfma_f32_16x16x32_f16 v[76:79], v[44:47], v[136:139], v[76:79]
	v_mfma_f32_16x16x32_f16 v[72:75], v[60:63], v[136:139], v[72:75]
	s_waitcnt lgkmcnt(3)
	v_mfma_f32_16x16x32_f16 v[28:31], v[44:47], v[144:147], v[28:31]
	v_mfma_f32_16x16x32_f16 v[24:27], v[60:63], v[144:147], v[24:27]
	s_waitcnt lgkmcnt(1)
	v_mfma_f32_16x16x32_f16 v[12:15], v[44:47], v[152:155], v[12:15]
	v_mfma_f32_16x16x32_f16 v[8:11], v[60:63], v[152:155], v[8:11]
	v_mfma_f32_16x16x32_f16 v[92:95], v[56:59], v[96:99], v[92:95]
	v_mfma_f32_16x16x32_f16 v[88:91], v[64:67], v[96:99], v[88:91]
	v_mfma_f32_16x16x32_f16 v[76:79], v[56:59], v[140:143], v[76:79]
	v_mfma_f32_16x16x32_f16 v[72:75], v[64:67], v[140:143], v[72:75]
	v_mfma_f32_16x16x32_f16 v[28:31], v[56:59], v[148:151], v[28:31]
	v_mfma_f32_16x16x32_f16 v[24:27], v[64:67], v[148:151], v[24:27]
	s_waitcnt lgkmcnt(0)
	v_mfma_f32_16x16x32_f16 v[12:15], v[56:59], v[156:159], v[12:15]
	v_mfma_f32_16x16x32_f16 v[8:11], v[64:67], v[156:159], v[8:11]
	s_setprio 0
	s_barrier
	s_add_i32 s76, s68, s54
	s_mov_b32 m0, s76
	s_nop 0
	global_load_lds_dwordx4 v120, s[80:81]
	s_add_i32 m0, s76, 0x2000
	s_nop 0
	global_load_lds_dwordx4 v122, s[80:81]
	ds_read_b128 v[44:47], v130 offset:32768
	ds_read_b128 v[56:59], v130 offset:33792
	ds_read_b128 v[60:63], v130 offset:34816
	ds_read_b128 v[64:67], v130 offset:35840
	s_waitcnt vmcnt(6)
	s_barrier
	s_setprio 1
	s_waitcnt lgkmcnt(3)
	v_mfma_f32_16x16x32_f16 v[84:87], v[44:47], v[68:71], v[84:87]
	v_mfma_f32_16x16x32_f16 v[52:55], v[44:47], v[136:139], v[52:55]
	s_waitcnt lgkmcnt(1)
	v_mfma_f32_16x16x32_f16 v[48:51], v[60:63], v[136:139], v[48:51]
	v_mfma_f32_16x16x32_f16 v[20:23], v[44:47], v[144:147], v[20:23]
	v_mfma_f32_16x16x32_f16 v[16:19], v[60:63], v[144:147], v[16:19]
	v_mfma_f32_16x16x32_f16 v[4:7], v[44:47], v[152:155], v[4:7]
	v_mfma_f32_16x16x32_f16 v[0:3], v[60:63], v[152:155], v[0:3]
	v_mfma_f32_16x16x32_f16 v[84:87], v[56:59], v[96:99], v[84:87]
	v_mfma_f32_16x16x32_f16 v[68:71], v[60:63], v[68:71], v[80:83]
	v_mfma_f32_16x16x32_f16 v[52:55], v[56:59], v[140:143], v[52:55]
	s_waitcnt lgkmcnt(0)
	v_mfma_f32_16x16x32_f16 v[48:51], v[64:67], v[140:143], v[48:51]
	v_mfma_f32_16x16x32_f16 v[20:23], v[56:59], v[148:151], v[20:23]
	v_mfma_f32_16x16x32_f16 v[16:19], v[64:67], v[148:151], v[16:19]
	v_mfma_f32_16x16x32_f16 v[4:7], v[56:59], v[156:159], v[4:7]
	v_mfma_f32_16x16x32_f16 v[0:3], v[64:67], v[156:159], v[0:3]
	v_mfma_f32_16x16x32_f16 v[68:71], v[64:67], v[96:99], v[68:71]
	s_setprio 0
	s_barrier
	s_add_i32 s76, 0, 0x10000
	s_mov_b32 m0, s57
	v_add_u32_e32 v64, s76, v128
	global_load_lds_dwordx4 v100, s[48:49]
	s_mov_b32 m0, s58
	s_nop 0
	global_load_lds_dwordx4 v104, s[48:49]
	s_mov_b32 m0, s59
	s_nop 0
	global_load_lds_dwordx4 v102, s[46:47]
	s_mov_b32 m0, s60
	s_nop 0
	global_load_lds_dwordx4 v106, s[46:47]
	ds_read_b128 v[44:47], v64
	ds_read_b128 v[56:59], v64 offset:1024
	ds_read_b128 v[60:63], v64 offset:2048
	ds_read_b128 v[64:67], v64 offset:3072
	ds_read_b128 v[80:83], v131 offset:49152
	ds_read_b128 v[96:99], v131 offset:50176
	ds_read_b128 v[136:139], v131 offset:51200
	ds_read_b128 v[140:143], v131 offset:52224
	ds_read_b128 v[144:147], v131 offset:53248
	ds_read_b128 v[148:151], v131 offset:54272
	ds_read_b128 v[152:155], v131 offset:55296
	ds_read_b128 v[156:159], v131 offset:56320
	s_barrier
	s_setprio 1
	s_waitcnt lgkmcnt(7)
	v_mfma_f32_16x16x32_f16 v[92:95], v[44:47], v[80:83], v[92:95]
	v_mfma_f32_16x16x32_f16 v[88:91], v[60:63], v[80:83], v[88:91]
	s_waitcnt lgkmcnt(5)
	v_mfma_f32_16x16x32_f16 v[76:79], v[44:47], v[136:139], v[76:79]
	v_mfma_f32_16x16x32_f16 v[72:75], v[60:63], v[136:139], v[72:75]
	s_waitcnt lgkmcnt(3)
	v_mfma_f32_16x16x32_f16 v[28:31], v[44:47], v[144:147], v[28:31]
	v_mfma_f32_16x16x32_f16 v[24:27], v[60:63], v[144:147], v[24:27]
	s_waitcnt lgkmcnt(1)
	v_mfma_f32_16x16x32_f16 v[12:15], v[44:47], v[152:155], v[12:15]
	v_mfma_f32_16x16x32_f16 v[8:11], v[60:63], v[152:155], v[8:11]
	v_mfma_f32_16x16x32_f16 v[92:95], v[56:59], v[96:99], v[92:95]
	v_mfma_f32_16x16x32_f16 v[88:91], v[64:67], v[96:99], v[88:91]
	v_mfma_f32_16x16x32_f16 v[76:79], v[56:59], v[140:143], v[76:79]
	v_mfma_f32_16x16x32_f16 v[72:75], v[64:67], v[140:143], v[72:75]
	v_mfma_f32_16x16x32_f16 v[28:31], v[56:59], v[148:151], v[28:31]
	v_mfma_f32_16x16x32_f16 v[24:27], v[64:67], v[148:151], v[24:27]
	s_waitcnt lgkmcnt(0)
	v_mfma_f32_16x16x32_f16 v[12:15], v[56:59], v[156:159], v[12:15]
	v_mfma_f32_16x16x32_f16 v[8:11], v[64:67], v[156:159], v[8:11]
	s_setprio 0
	s_barrier
	s_add_i32 s48, 0, 0x14000
	s_add_u32 s46, s46, s10
	s_addc_u32 s47, s47, s11
	s_mov_b32 m0, s61
	v_add_u32_e32 v64, s48, v128
	global_load_lds_dwordx4 v102, s[46:47]
	s_mov_b32 m0, s62
	s_nop 0
	global_load_lds_dwordx4 v106, s[46:47]
	ds_read_b128 v[44:47], v64
	ds_read_b128 v[56:59], v64 offset:1024
	ds_read_b128 v[60:63], v64 offset:2048
	ds_read_b128 v[64:67], v64 offset:3072
	s_waitcnt vmcnt(6)
	s_barrier
	s_setprio 1
	s_waitcnt lgkmcnt(3)
	v_mfma_f32_16x16x32_f16 v[84:87], v[44:47], v[80:83], v[84:87]
	v_mfma_f32_16x16x32_f16 v[52:55], v[44:47], v[136:139], v[52:55]
	s_waitcnt lgkmcnt(1)
	v_mfma_f32_16x16x32_f16 v[48:51], v[60:63], v[136:139], v[48:51]
	v_mfma_f32_16x16x32_f16 v[20:23], v[44:47], v[144:147], v[20:23]
	v_mfma_f32_16x16x32_f16 v[16:19], v[60:63], v[144:147], v[16:19]
	v_mfma_f32_16x16x32_f16 v[4:7], v[44:47], v[152:155], v[4:7]
	v_mfma_f32_16x16x32_f16 v[0:3], v[60:63], v[152:155], v[0:3]
	v_mfma_f32_16x16x32_f16 v[84:87], v[56:59], v[96:99], v[84:87]
	v_mfma_f32_16x16x32_f16 v[68:71], v[60:63], v[80:83], v[68:71]
	v_mfma_f32_16x16x32_f16 v[52:55], v[56:59], v[140:143], v[52:55]
	s_waitcnt lgkmcnt(0)
	v_mfma_f32_16x16x32_f16 v[48:51], v[64:67], v[140:143], v[48:51]
	v_mfma_f32_16x16x32_f16 v[20:23], v[56:59], v[148:151], v[20:23]
	v_mfma_f32_16x16x32_f16 v[16:19], v[64:67], v[148:151], v[16:19]
	v_mfma_f32_16x16x32_f16 v[4:7], v[56:59], v[156:159], v[4:7]
	v_mfma_f32_16x16x32_f16 v[0:3], v[64:67], v[156:159], v[0:3]
	v_mfma_f32_16x16x32_f16 v[68:71], v[64:67], v[96:99], v[68:71]
	s_setprio 0
	s_barrier
	s_mov_b32 m0, s64
	s_nop 0
	global_load_lds_dwordx4 v100, s[82:83]
	s_mov_b32 m0, s65
	s_add_i32 s46, s76, s54
	global_load_lds_dwordx4 v104, s[82:83]
	s_mov_b32 m0, s46
	s_nop 0
	global_load_lds_dwordx4 v102, s[84:85]
	s_add_i32 m0, s46, 0x2000
	s_nop 0
	global_load_lds_dwordx4 v106, s[84:85]
	ds_read_b128 v[44:47], v132
	ds_read_b128 v[56:59], v132 offset:1024
	ds_read_b128 v[60:63], v132 offset:2048
	ds_read_b128 v[64:67], v132 offset:3072
	ds_read_b128 v[80:83], v133
	ds_read_b128 v[96:99], v133 offset:1024
	ds_read_b128 v[136:139], v133 offset:2048
	ds_read_b128 v[140:143], v133 offset:3072
	ds_read_b128 v[144:147], v133 offset:4096
	ds_read_b128 v[148:151], v133 offset:5120
	ds_read_b128 v[152:155], v133 offset:6144
	ds_read_b128 v[156:159], v133 offset:7168
	s_barrier
	s_setprio 1
	s_waitcnt lgkmcnt(7)
	v_mfma_f32_16x16x32_f16 v[92:95], v[44:47], v[80:83], v[92:95]
	v_mfma_f32_16x16x32_f16 v[88:91], v[60:63], v[80:83], v[88:91]
	s_waitcnt lgkmcnt(5)
	v_mfma_f32_16x16x32_f16 v[76:79], v[44:47], v[136:139], v[76:79]
	v_mfma_f32_16x16x32_f16 v[72:75], v[60:63], v[136:139], v[72:75]
	s_waitcnt lgkmcnt(3)
	v_mfma_f32_16x16x32_f16 v[28:31], v[44:47], v[144:147], v[28:31]
	v_mfma_f32_16x16x32_f16 v[24:27], v[60:63], v[144:147], v[24:27]
	s_waitcnt lgkmcnt(1)
	v_mfma_f32_16x16x32_f16 v[12:15], v[44:47], v[152:155], v[12:15]
	v_mfma_f32_16x16x32_f16 v[8:11], v[60:63], v[152:155], v[8:11]
	v_mfma_f32_16x16x32_f16 v[92:95], v[56:59], v[96:99], v[92:95]
	v_mfma_f32_16x16x32_f16 v[88:91], v[64:67], v[96:99], v[88:91]
	v_mfma_f32_16x16x32_f16 v[76:79], v[56:59], v[140:143], v[76:79]
	v_mfma_f32_16x16x32_f16 v[72:75], v[64:67], v[140:143], v[72:75]
	v_mfma_f32_16x16x32_f16 v[28:31], v[56:59], v[148:151], v[28:31]
	v_mfma_f32_16x16x32_f16 v[24:27], v[64:67], v[148:151], v[24:27]
	s_waitcnt lgkmcnt(0)
	v_mfma_f32_16x16x32_f16 v[12:15], v[56:59], v[156:159], v[12:15]
	v_mfma_f32_16x16x32_f16 v[8:11], v[64:67], v[156:159], v[8:11]
	s_setprio 0
	s_barrier
	s_add_i32 s46, s48, s54
	s_mov_b32 m0, s46
	s_nop 0
	global_load_lds_dwordx4 v102, s[86:87]
	s_add_i32 m0, s46, 0x2000
	s_nop 0
	global_load_lds_dwordx4 v106, s[86:87]
	ds_read_b128 v[44:47], v134
	ds_read_b128 v[56:59], v134 offset:1024
	ds_read_b128 v[60:63], v134 offset:2048
	ds_read_b128 v[64:67], v134 offset:3072
	s_waitcnt vmcnt(6)
	s_barrier
	s_setprio 1
	s_waitcnt lgkmcnt(3)
	v_mfma_f32_16x16x32_f16 v[84:87], v[44:47], v[80:83], v[84:87]
	s_waitcnt lgkmcnt(1)
	v_mfma_f32_16x16x32_f16 v[68:71], v[60:63], v[80:83], v[68:71]
	v_mfma_f32_16x16x32_f16 v[52:55], v[44:47], v[136:139], v[52:55]
	v_mfma_f32_16x16x32_f16 v[48:51], v[60:63], v[136:139], v[48:51]
	v_mfma_f32_16x16x32_f16 v[20:23], v[44:47], v[144:147], v[20:23]
	v_mfma_f32_16x16x32_f16 v[16:19], v[60:63], v[144:147], v[16:19]
	v_mfma_f32_16x16x32_f16 v[4:7], v[44:47], v[152:155], v[4:7]
	v_mfma_f32_16x16x32_f16 v[0:3], v[60:63], v[152:155], v[0:3]
	v_mfma_f32_16x16x32_f16 v[84:87], v[56:59], v[96:99], v[84:87]
	s_waitcnt lgkmcnt(0)
	v_mfma_f32_16x16x32_f16 v[80:83], v[64:67], v[96:99], v[68:71]
	v_mfma_f32_16x16x32_f16 v[52:55], v[56:59], v[140:143], v[52:55]
	v_mfma_f32_16x16x32_f16 v[48:51], v[64:67], v[140:143], v[48:51]
	v_mfma_f32_16x16x32_f16 v[20:23], v[56:59], v[148:151], v[20:23]
	v_mfma_f32_16x16x32_f16 v[16:19], v[64:67], v[148:151], v[16:19]
	v_mfma_f32_16x16x32_f16 v[4:7], v[56:59], v[156:159], v[4:7]
	v_mfma_f32_16x16x32_f16 v[0:3], v[64:67], v[156:159], v[0:3]
	s_setprio 0
	s_add_i32 s75, s75, 3
	s_add_u32 s44, s44, 0x180
	s_addc_u32 s45, s45, 0
	s_cmp_ge_i32 s75, s66
	s_cbranch_scc1 .Lrot_exit_mlp1
	s_add_u32 s78, s40, s44
	s_addc_u32 s79, s41, s45
	s_add_u32 s80, s42, s44
	s_addc_u32 s81, s43, s45
	s_add_u32 s46, s40, s44
	s_addc_u32 s47, s41, s45
	s_add_u32 s46, s46, 0x180
	s_addc_u32 s47, s47, 0
	s_add_u32 s48, s42, s44
	s_addc_u32 s49, s43, s45
	s_add_u32 s76, s48, 0x180
	s_addc_u32 s77, s49, 0
	s_cmp_eq_u32 s67, s75
	s_cselect_b32 s49, s7, s47
	s_cselect_b32 s48, s6, s46
	s_cselect_b32 s47, s5, s77
	s_cselect_b32 s46, s4, s76
	s_add_u32 s82, s48, 0x80
	s_addc_u32 s83, s49, 0
	s_add_u32 s84, s46, 0x80
	s_addc_u32 s85, s47, 0
	s_add_u32 s86, s84, s10
	s_addc_u32 s87, s85, s11
	s_add_i32 s76, s19, s54
	s_barrier
	s_branch .LBB5_55

.LBB6_22:
	s_mov_b32 m0, s68
	s_nop 0
	global_load_lds_dwordx4 v106, s[72:73]
	s_add_i32 m0, s68, 0x2000
	s_nop 0
	global_load_lds_dwordx4 v108, s[72:73]
	ds_read_b128 v[132:135], v131 offset:16384
	ds_read_b128 v[136:139], v131 offset:17408
	ds_read_b128 v[140:143], v131 offset:18432
	ds_read_b128 v[144:147], v131 offset:19456
	ds_read_b128 v[148:151], v182
	ds_read_b128 v[152:155], v182 offset:1024
	ds_read_b128 v[156:159], v182 offset:2048
	ds_read_b128 v[160:163], v182 offset:3072
	ds_read_b128 v[164:167], v182 offset:4096
	ds_read_b128 v[168:171], v182 offset:5120
	ds_read_b128 v[172:175], v182 offset:6144
	ds_read_b128 v[176:179], v182 offset:7168
	s_barrier
	s_setprio 1
	s_waitcnt lgkmcnt(7)
	v_mfma_f32_16x16x32_f16 v[40:43], v[132:135], v[148:151], v[40:43]
	v_mfma_f32_16x16x32_f16 v[44:47], v[140:143], v[148:151], v[44:47]
	s_waitcnt lgkmcnt(5)
	v_mfma_f32_16x16x32_f16 v[32:35], v[132:135], v[156:159], v[32:35]
	v_mfma_f32_16x16x32_f16 v[28:31], v[140:143], v[156:159], v[28:31]
	s_waitcnt lgkmcnt(3)
	v_mfma_f32_16x16x32_f16 v[20:23], v[132:135], v[164:167], v[20:23]
	v_mfma_f32_16x16x32_f16 v[16:19], v[140:143], v[164:167], v[16:19]
	s_waitcnt lgkmcnt(1)
	v_mfma_f32_16x16x32_f16 v[8:11], v[132:135], v[172:175], v[8:11]
	v_mfma_f32_16x16x32_f16 v[4:7], v[140:143], v[172:175], v[4:7]
	v_mfma_f32_16x16x32_f16 v[40:43], v[136:139], v[152:155], v[40:43]
	v_mfma_f32_16x16x32_f16 v[44:47], v[144:147], v[152:155], v[44:47]
	v_mfma_f32_16x16x32_f16 v[32:35], v[136:139], v[160:163], v[32:35]
	v_mfma_f32_16x16x32_f16 v[28:31], v[144:147], v[160:163], v[28:31]
	v_mfma_f32_16x16x32_f16 v[20:23], v[136:139], v[168:171], v[20:23]
	v_mfma_f32_16x16x32_f16 v[16:19], v[144:147], v[168:171], v[16:19]
	s_waitcnt lgkmcnt(0)
	v_mfma_f32_16x16x32_f16 v[8:11], v[136:139], v[176:179], v[8:11]
	v_mfma_f32_16x16x32_f16 v[4:7], v[144:147], v[176:179], v[4:7]
	s_setprio 0
	s_barrier
	s_add_i32 m0, s47, 0x18000
	s_nop 0
	global_load_lds_dwordx4 v110, s[74:75]
	s_add_i32 m0, s47, 0x1a000
	s_nop 0
	global_load_lds_dwordx4 v112, s[74:75]
	s_add_i32 m0, s47, 0x1c000
	s_nop 0
	global_load_lds_dwordx4 v114, s[74:75]
	ds_read_b128 v[132:135], v131 offset:20480
	ds_read_b128 v[136:139], v131 offset:21504
	s_cmp_lg_u32 s65, 0
	s_cbranch_scc1 .Lm2_norm_0
	s_mul_i32 s70, s58, 0xc0
	v_add_u32_e32 v234, s70, v129
	v_ashrrev_i32_e32 v235, 31, v234
	v_lshlrev_b64 v[234:235], 2, v[234:235]
	v_lshl_add_u64 v[234:235], s[18:19], 0, v[234:235]
	global_load_dwordx4 v[222:225], v[234:235], off
	global_load_dwordx4 v[226:229], v[234:235], off offset:64
	global_load_dwordx4 v[230:233], v[234:235], off offset:128
	global_load_dwordx2 v[198:199], v[190:191], off
	global_load_dwordx2 v[200:201], v[190:191], off offset:32
	global_load_dwordx2 v[202:203], v[190:191], off offset:64
	global_load_dwordx2 v[204:205], v[192:193], off
	s_waitcnt vmcnt(12)
	s_branch .Lm2_join_0

.Lm2_join_0:
	s_barrier
	s_setprio 1
	s_waitcnt lgkmcnt(1)
	v_mfma_f32_16x16x32_f16 v[36:39], v[132:135], v[148:151], v[36:39]
	v_mfma_f32_16x16x32_f16 v[24:27], v[132:135], v[156:159], v[24:27]
	v_mfma_f32_16x16x32_f16 v[12:15], v[132:135], v[164:167], v[12:15]
	v_mfma_f32_16x16x32_f16 v[0:3], v[132:135], v[172:175], v[0:3]
	s_waitcnt lgkmcnt(0)
	v_mfma_f32_16x16x32_f16 v[36:39], v[136:139], v[152:155], v[36:39]
	v_mfma_f32_16x16x32_f16 v[24:27], v[136:139], v[160:163], v[24:27]
	v_mfma_f32_16x16x32_f16 v[12:15], v[136:139], v[168:171], v[12:15]
	v_mfma_f32_16x16x32_f16 v[0:3], v[136:139], v[176:179], v[0:3]
	s_setprio 0
	s_barrier
	s_mov_b32 m0, s47
	s_nop 0
	global_load_lds_dwordx4 v48, s[66:67]
	s_mov_b32 m0, s48
	s_nop 0
	global_load_lds_dwordx4 v52, s[66:67]
	ds_read_b128 v[132:135], v131 offset:57344
	ds_read_b128 v[136:139], v131 offset:58368
	ds_read_b128 v[140:143], v131 offset:59392
	ds_read_b128 v[144:147], v131 offset:60416
	ds_read_b128 v[148:151], v182 offset:40960
	ds_read_b128 v[152:155], v182 offset:41984
	ds_read_b128 v[156:159], v182 offset:43008
	ds_read_b128 v[160:163], v182 offset:44032
	ds_read_b128 v[164:167], v182 offset:45056
	ds_read_b128 v[168:171], v182 offset:46080
	ds_read_b128 v[172:175], v182 offset:47104
	ds_read_b128 v[176:179], v182 offset:48128
	s_barrier
	s_setprio 1
	s_waitcnt lgkmcnt(7)
	v_mfma_f32_16x16x32_f16 v[40:43], v[132:135], v[148:151], v[40:43]
	v_mfma_f32_16x16x32_f16 v[44:47], v[140:143], v[148:151], v[44:47]
	s_waitcnt lgkmcnt(5)
	v_mfma_f32_16x16x32_f16 v[32:35], v[132:135], v[156:159], v[32:35]
	v_mfma_f32_16x16x32_f16 v[28:31], v[140:143], v[156:159], v[28:31]
	s_waitcnt lgkmcnt(3)
	v_mfma_f32_16x16x32_f16 v[20:23], v[132:135], v[164:167], v[20:23]
	v_mfma_f32_16x16x32_f16 v[16:19], v[140:143], v[164:167], v[16:19]
	s_waitcnt lgkmcnt(1)
	v_mfma_f32_16x16x32_f16 v[8:11], v[132:135], v[172:175], v[8:11]
	v_mfma_f32_16x16x32_f16 v[4:7], v[140:143], v[172:175], v[4:7]
	v_mfma_f32_16x16x32_f16 v[40:43], v[136:139], v[152:155], v[40:43]
	v_mfma_f32_16x16x32_f16 v[44:47], v[144:147], v[152:155], v[44:47]
	v_mfma_f32_16x16x32_f16 v[32:35], v[136:139], v[160:163], v[32:35]
	v_mfma_f32_16x16x32_f16 v[28:31], v[144:147], v[160:163], v[28:31]
	v_mfma_f32_16x16x32_f16 v[20:23], v[136:139], v[168:171], v[20:23]
	v_mfma_f32_16x16x32_f16 v[16:19], v[144:147], v[168:171], v[16:19]
	s_waitcnt lgkmcnt(0)
	v_mfma_f32_16x16x32_f16 v[8:11], v[136:139], v[176:179], v[8:11]
	v_mfma_f32_16x16x32_f16 v[4:7], v[144:147], v[176:179], v[4:7]
	s_setprio 0
	s_barrier
	s_mov_b32 m0, s49
	s_nop 0
	global_load_lds_dwordx4 v50, s[30:31]
	s_mov_b32 m0, s50
	s_nop 0
	global_load_lds_dwordx4 v54, s[30:31]
	s_mov_b32 m0, s51
	s_nop 0
	global_load_lds_dwordx4 v56, s[30:31]
	ds_read_b128 v[132:135], v131 offset:61440
	ds_read_b128 v[136:139], v131 offset:62464
	s_cmp_lg_u32 s65, 0
	s_cbranch_scc1 .Lm2_norm_1
	global_load_dwordx2 v[206:207], v[192:193], off offset:32
	global_load_dwordx2 v[208:209], v[192:193], off offset:64
	global_load_dwordx2 v[210:211], v[194:195], off
	global_load_dwordx2 v[212:213], v[194:195], off offset:32
	s_waitcnt vmcnt(16)
	s_branch .Lm2_join_1

.Lm2_join_1:
	s_barrier
	s_setprio 1
	s_waitcnt lgkmcnt(1)
	v_mfma_f32_16x16x32_f16 v[36:39], v[132:135], v[148:151], v[36:39]
	v_mfma_f32_16x16x32_f16 v[24:27], v[132:135], v[156:159], v[24:27]
	v_mfma_f32_16x16x32_f16 v[12:15], v[132:135], v[164:167], v[12:15]
	v_mfma_f32_16x16x32_f16 v[0:3], v[132:135], v[172:175], v[0:3]
	s_waitcnt lgkmcnt(0)
	v_mfma_f32_16x16x32_f16 v[36:39], v[136:139], v[152:155], v[36:39]
	v_mfma_f32_16x16x32_f16 v[24:27], v[136:139], v[160:163], v[24:27]
	v_mfma_f32_16x16x32_f16 v[12:15], v[136:139], v[168:171], v[12:15]
	v_mfma_f32_16x16x32_f16 v[0:3], v[136:139], v[176:179], v[0:3]
	s_setprio 0
	s_barrier
	s_mov_b32 m0, s54
	v_add_u32_e32 v131, s62, v127
	global_load_lds_dwordx4 v48, s[76:77]
	s_mov_b32 m0, s55
	s_nop 0
	global_load_lds_dwordx4 v52, s[76:77]
	ds_read_b128 v[132:135], v130
	ds_read_b128 v[136:139], v130 offset:1024
	ds_read_b128 v[140:143], v130 offset:2048
	ds_read_b128 v[144:147], v130 offset:3072
	ds_read_b128 v[148:151], v131
	ds_read_b128 v[152:155], v131 offset:1024
	ds_read_b128 v[156:159], v131 offset:2048
	ds_read_b128 v[160:163], v131 offset:3072
	ds_read_b128 v[164:167], v131 offset:4096
	ds_read_b128 v[168:171], v131 offset:5120
	ds_read_b128 v[172:175], v131 offset:6144
	ds_read_b128 v[176:179], v131 offset:7168
	s_barrier
	s_setprio 1
	s_waitcnt lgkmcnt(7)
	v_mfma_f32_16x16x32_f16 v[40:43], v[132:135], v[148:151], v[40:43]
	v_mfma_f32_16x16x32_f16 v[44:47], v[140:143], v[148:151], v[44:47]
	s_waitcnt lgkmcnt(5)
	v_mfma_f32_16x16x32_f16 v[32:35], v[132:135], v[156:159], v[32:35]
	v_mfma_f32_16x16x32_f16 v[28:31], v[140:143], v[156:159], v[28:31]
	s_waitcnt lgkmcnt(3)
	v_mfma_f32_16x16x32_f16 v[20:23], v[132:135], v[164:167], v[20:23]
	v_mfma_f32_16x16x32_f16 v[16:19], v[140:143], v[164:167], v[16:19]
	s_waitcnt lgkmcnt(1)
	v_mfma_f32_16x16x32_f16 v[8:11], v[132:135], v[172:175], v[8:11]
	v_mfma_f32_16x16x32_f16 v[4:7], v[140:143], v[172:175], v[4:7]
	v_mfma_f32_16x16x32_f16 v[40:43], v[136:139], v[152:155], v[40:43]
	v_mfma_f32_16x16x32_f16 v[44:47], v[144:147], v[152:155], v[44:47]
	v_mfma_f32_16x16x32_f16 v[32:35], v[136:139], v[160:163], v[32:35]
	v_mfma_f32_16x16x32_f16 v[28:31], v[144:147], v[160:163], v[28:31]
	v_mfma_f32_16x16x32_f16 v[20:23], v[136:139], v[168:171], v[20:23]
	v_mfma_f32_16x16x32_f16 v[16:19], v[144:147], v[168:171], v[16:19]
	s_waitcnt lgkmcnt(0)
	v_mfma_f32_16x16x32_f16 v[8:11], v[136:139], v[176:179], v[8:11]
	v_mfma_f32_16x16x32_f16 v[4:7], v[144:147], v[176:179], v[4:7]
	s_setprio 0
	s_barrier
	s_mov_b32 m0, s56
	s_nop 0
	global_load_lds_dwordx4 v50, s[78:79]
	s_add_i32 m0, s56, 0x2000
	s_nop 0
	global_load_lds_dwordx4 v54, s[78:79]
	s_add_i32 m0, s56, 0x4000
	s_nop 0
	global_load_lds_dwordx4 v56, s[78:79]
	ds_read_b128 v[132:135], v130 offset:4096
	ds_read_b128 v[136:139], v130 offset:5120
	s_cmp_lg_u32 s65, 0
	s_cbranch_scc1 .Lm2_norm_2
	global_load_dwordx2 v[214:215], v[194:195], off offset:64
	global_load_dwordx2 v[216:217], v[196:197], off
	global_load_dwordx2 v[218:219], v[196:197], off offset:32
	global_load_dwordx2 v[220:221], v[196:197], off offset:64
	s_waitcnt vmcnt(13)
	s_branch .Lm2_join_2
